# final6 + K-fragment register prefetch across the step barrier in both diff-attention loops: 4-slot LDS ring staged 3 tiles ahead, K(t+1) b128 reads issued in the PV shadow of step t into dedicated VGP
# baseline (speedup 1.0000x reference)
; #define AT_BAR() asm volatile("s_waitcnt vmcnt(0) lgkmcnt(0)\n\ts_barrier" ::: "memory")
; DI int at_v_rd_base(int lane) { return ((lane & 3) << 3) | (((lane >> 2) & 3) << 6) | (((lane >> 4) & 1) << 5) | (((lane >> 5) & 1) << 8); }
; DI void attn_unit_diff(const Ctx& C, int l, int b, int h, int j) {
;     ...
;     AT_BAR();
;     unsigned lb0, lb1;
;     { const int kv = wid >> 2;
;       if (kv == 0) { const int rl = lane >> 4, cp = lane & 15; lb0 = (unsigned)(rl * (INW * 2) + ((cp ^ (rl & 7)) * 16)); lb1 = (unsigned)(rl * (INW * 2) + ((cp ^ ((4 + rl) & 7)) * 16)); }
;       else { lb0 = (unsigned)(((lane & 31) >> 2) * (INW * 2) + ((lane >> 5) * 32 + (lane & 3) * 8) * 2); lb1 = lb0; } }
;     at_stage1(C.lds, projb, kcolB, vcolB, 0, 0, wid, lb0, lb1);
;     at_stage1(C.lds, projb, kcolB, vcolB, 1, 1, wid, lb0, lb1);
;     __builtin_amdgcn_sched_barrier(0);
;     bf16x8 qr[8];
;     { const bf16_t* qp = proj + (rowb + qpos) * INW + qcol + 8 * hi;
; #pragma unroll
;       for (int s = 0; s < KS; ++s) qr[s] = *(const bf16x8*)(qp + 16 * s); }
;     for (int i = wid * 64 + lane; i < TABB_N; i += NTHREADS) tabl[i] = tabg[i];
;     f32x16 o[4], ol = {}; float m_run = 0.f; bool first = true;
; #pragma unroll
;     for (int d0 = 0; d0 < 4; ++d0) o[d0] = f32x16{};
;     const bf16x8 ones = {16256, 16256, 16256, 16256, 16256, 16256, 16256, 16256};
;     asm volatile("s_waitcnt vmcnt(0) lgkmcnt(0)\n\ts_barrier" ::: "memory");
;     const float cfar = tabl[0];
;     const int vrd = at_v_rd_base(lane);
;     for (int sd = 0; sd < nt; ++sd) {
;         const int slot = sd % 3;
;         const bool staged = sd + 2 < nt;
;         if (staged) at_stage1(C.lds, projb, kcolB, vcolB, sd + 2, (sd + 2) % 3, wid, lb0, lb1);
.LBB0_785:
	s_or_b64 exec, exec, s[38:39]
	s_add_i32 s50, 0, 0x20000
	s_lshr_b32 s28, s97, 4
	s_lshl_b32 s66, s49, 1
	v_readlane_b32 s38, v252, 22
	s_waitcnt vmcnt(0) lgkmcnt(0)
	s_barrier
	v_mov_b32_e32 v4, s50
	s_and_b32 s28, s28, 7
	s_or_b32 s67, s66, s38
	s_waitcnt lgkmcnt(0)
	ds_read_b32 v158, v4
	v_and_b32_e32 v4, 24, v8
	v_and_b32_e32 v7, 0x100, v8
	v_lshlrev_b32_e32 v8, 4, v156
	v_readlane_b32 s38, v252, 26
	s_lshl_b32 s28, s28, 8
	v_lshlrev_b32_e32 v145, 4, v154
	v_add_u32_e32 v9, s38, v8
	v_readlane_b32 s38, v252, 23
	v_lshlrev_b32_e32 v11, 4, v155
	v_lshlrev_b32_e32 v15, 2, v154
	s_add_i32 s88, s55, 0xfffffe90
	s_add_i32 s38, s38, s52
	s_add_i32 s91, 0, 0x4000
	s_add_i32 s52, s48, s28
	v_mov_b32_e32 v3, v1
	v_and_b32_e32 v5, 0xc0, v145
	v_lshlrev_b32_e32 v6, 1, v154
	v_lshlrev_b32_e32 v10, 8, v155
	v_and_b32_e32 v11, 0x70, v11
	v_add_u32_e32 v14, 0x60, v9
	v_xor_b32_e32 v157, 0x80, v15
	v_add_lshl_u32 v15, s38, v155, 2
	s_add_u32 s38, s96, s42
	v_and_b32_e32 v6, 32, v6
	v_add_u32_e32 v12, 32, v9
	v_add_u32_e32 v13, 64, v9
	v_sub_u32_e32 v159, v8, v15
	v_add3_u32 v5, v7, s91, v5
	v_xad_u32 v164, v14, v11, v10
	v_lshl_add_u64 v[2:3], s[42:43], 0, v[2:3]
	s_addc_u32 s39, s89, s43
	v_mov_b32_e32 v14, v1
	v_mov_b32_e32 v15, v1
	v_add3_u32 v160, v5, v6, v4
	v_xad_u32 v161, v9, v11, v10
	v_xad_u32 v162, v12, v11, v10
	v_xad_u32 v163, v13, v11, v10
	v_lshl_add_u64 v[146:147], s[70:71], 0, v[2:3]
	v_lshl_add_u64 v[148:149], s[72:73], 0, v[2:3]
	v_lshl_add_u64 v[150:151], s[38:39], 0, v[0:1]
	s_lshl_b32 s95, s49, 16
	v_mov_b32_e32 v0, v1
	v_mov_b32_e32 v2, v1
	v_mov_b32_e32 v3, v1
	v_mov_b32_e32 v4, v1
	v_mov_b32_e32 v5, v1
	v_mov_b32_e32 v6, v1
	v_mov_b32_e32 v7, v1
	v_mov_b32_e32 v8, v1
	v_mov_b32_e32 v9, v1
	v_mov_b32_e32 v10, v1
	v_mov_b32_e32 v11, v1
	v_mov_b32_e32 v12, v1
	v_mov_b32_e32 v13, v1
	v_mov_b64_e32 v[78:79], v[14:15]
	v_mov_b64_e32 v[62:63], v[14:15]
	v_mov_b64_e32 v[46:47], v[14:15]
	v_mov_b64_e32 v[30:31], v[14:15]
	v_mov_b64_e32 v[94:95], v[14:15]
	s_mov_b32 s79, 2
	s_add_i32 s95, s95, 0x10000
	s_mov_b32 s48, 0
	v_mov_b32_e32 v165, 0
	s_mov_b64 s[38:39], -1
	s_mov_b32 s49, 0
	v_mov_b64_e32 v[76:77], v[12:13]
	v_mov_b64_e32 v[74:75], v[10:11]
	v_mov_b64_e32 v[72:73], v[8:9]
	v_mov_b64_e32 v[70:71], v[6:7]
	v_mov_b64_e32 v[68:69], v[4:5]
	v_mov_b64_e32 v[66:67], v[2:3]
	v_mov_b64_e32 v[64:65], v[0:1]
	v_mov_b64_e32 v[60:61], v[12:13]
	v_mov_b64_e32 v[58:59], v[10:11]
	v_mov_b64_e32 v[56:57], v[8:9]
	v_mov_b64_e32 v[54:55], v[6:7]
	v_mov_b64_e32 v[52:53], v[4:5]
	v_mov_b64_e32 v[50:51], v[2:3]
	v_mov_b64_e32 v[48:49], v[0:1]
	v_mov_b64_e32 v[44:45], v[12:13]
	v_mov_b64_e32 v[42:43], v[10:11]
	v_mov_b64_e32 v[40:41], v[8:9]
	v_mov_b64_e32 v[38:39], v[6:7]
	v_mov_b64_e32 v[36:37], v[4:5]
	v_mov_b64_e32 v[34:35], v[2:3]
	v_mov_b64_e32 v[32:33], v[0:1]
	v_mov_b64_e32 v[28:29], v[12:13]
	v_mov_b64_e32 v[26:27], v[10:11]
	v_mov_b64_e32 v[24:25], v[8:9]
	v_mov_b64_e32 v[22:23], v[6:7]
	v_mov_b64_e32 v[20:21], v[4:5]
	v_mov_b64_e32 v[18:19], v[2:3]
	v_mov_b64_e32 v[16:17], v[0:1]
	v_mov_b64_e32 v[92:93], v[12:13]
	v_mov_b64_e32 v[90:91], v[10:11]
	v_mov_b64_e32 v[88:89], v[8:9]
	v_mov_b64_e32 v[86:87], v[6:7]
	v_mov_b64_e32 v[84:85], v[4:5]
	v_mov_b64_e32 v[82:83], v[2:3]
	v_mov_b64_e32 v[80:81], v[0:1]
	s_mov_b32 s94, 0
	s_waitcnt vmcnt(0)
	s_mul_hi_u32 s57, s79, 0xaaaaaaab
	s_lshr_b32 s57, s57, 1
	s_mul_i32 s57, s57, 0x18000
	s_sub_i32 s58, s60, s57
	s_sub_i32 s59, s61, s57
	s_add_i32 s58, s49, s58
	v_lshl_add_u64 v[2:3], v[150:151], 0, s[52:53]
	s_sub_i32 s80, s4, s57
	s_add_i32 m0, s90, s58
	v_lshl_add_u64 v[4:5], v[2:3], 0, s[36:37]
	s_add_i32 s58, s49, s59
	s_sub_i32 s57, s5, s57
	global_load_lds_dwordx4 v[4:5], off
	v_lshl_add_u64 v[4:5], v[148:149], 0, s[52:53]
	s_add_i32 m0, s90, s58
	s_add_i32 s58, s49, s80
	global_load_lds_dwordx4 v[4:5], off
	v_lshl_add_u64 v[2:3], v[2:3], 0, s[24:25]
	s_add_i32 m0, s90, s58
	s_add_i32 s57, s49, s57
	global_load_lds_dwordx4 v[2:3], off
	v_lshl_add_u64 v[2:3], v[146:147], 0, s[52:53]
	s_add_i32 m0, s90, s57
	s_nop 0
	global_load_lds_dwordx4 v[2:3], off
	v_lshl_add_u64 v[146:147], v[146:147], 0, s[68:69]
	v_lshl_add_u64 v[148:149], v[148:149], 0, s[68:69]
	v_lshl_add_u64 v[150:151], v[150:151], 0, s[68:69]
	ds_read_b128 v[186:189], v161
	ds_read_b128 v[190:193], v161 offset:8192
	ds_read_b128 v[202:205], v162
	ds_read_b128 v[206:209], v162 offset:8192
	ds_read_b128 v[210:213], v163
	ds_read_b128 v[214:217], v163 offset:8192
	ds_read_b128 v[218:221], v164
	ds_read_b128 v[222:225], v164 offset:8192
	s_branch .LBB0_787

; DI void attn_unit_diff(const Ctx& C, int l, int b, int h, int j) {
;     ...
;     for (int sd = 0; sd < nt; ++sd) {
;         const int slot = sd % 3;
;         const bool staged = sd + 2 < nt;
;         if (staged) at_stage1(C.lds, projb, kcolB, vcolB, sd + 2, (sd + 2) % 3, wid, lb0, lb1);
;         if (sd <= cw) {
.LBB0_787:
	s_add_i32 s101, s94, 1
	s_cmp_ge_u32 s101, s66
	s_cselect_b64 s[40:41], -1, 0
	s_and_b64 vcc, exec, s[40:41]
	s_cbranch_vccz .LBB0_791
	s_cmp_gt_u32 s94, s67
	s_cbranch_scc0 .LBB0_792

; #define LAS __attribute__((address_space(3)))
; #define MFMA32(a, b, c) __builtin_amdgcn_mfma_f32_32x32x16_bf16((a), (b), (c), 0, 0, 0)
;     __device__ __forceinline__ void init(const void* A_, const void* B_, int lda_, int ldb_, int M, unsigned mask_, int G_, int c_) { A = (const char*)A_; B = (const char*)B_; lda = lda_; ldb = ldb_; nM = M / BM; mask = mask_; nN = __builtin_popcount(mask_); nwg = nM * nN; G = G_; c = c_; }
;     __device__ __forceinline__ void init(f32x4 (&acc)[2][2][4][2], const Unit& u, int wr, int wc, int fr, int fq) const { u32x4 old[2][4][2]; init_load(old, u, wr, wc, fr, fq); init_finish(acc, old); }
; template <int KS> DI void at_qk(f32x16& p0, f32x16& p1, LAS const unsigned char* Kt, int mapB, const bf16x8 (&qr)[8], float init, int r32, int hi) {
; #pragma unroll
;     for (int i = 0; i < 16; ++i) { p0[i] = init; p1[i] = init; }
;     bf16x8 kb[KS][2];
; #pragma unroll
;     for (int d0 = 0; d0 < KS; ++d0) { const int cb = mapB + (d0 * 16 + hi * 8) * 2;
;         kb[d0][0] = *(const LAS bf16x8*)(Kt + AT_KSWZ(r32, cb)); kb[d0][1] = *(const LAS bf16x8*)(Kt + AT_KSWZ(32 + r32, cb)); }
;     __builtin_amdgcn_sched_barrier(0);
; #pragma unroll
;     for (int d0 = 0; d0 < KS; ++d0) { p0 = MFMA32(kb[d0][0], qr[d0], p0); p1 = MFMA32(kb[d0][1], qr[d0], p1); }
; }
; DI void attn_unit_diff(const Ctx& C, int l, int b, int h, int j) {
;     ...
;         if (staged) at_stage1(C.lds, projb, kcolB, vcolB, sd + 2, (sd + 2) % 3, wid, lb0, lb1);
;         if (sd <= cw) {
;             LAS const unsigned char* Kt = C.lds + slot * 32768;
;             const int vb = (int)(size_t)(Kt + 16384) + vrd;
;             const bool nearb = (sd * 64 + 63 - q0w) > -305;
;             LAS const float* tabp = tabl + (sd * 64 - qpos + TABB_OFF + 4 * hi);
;             f32x16 p0, p1;
;             at_qk<KS>(p0, p1, Kt, g * 128, qr, (nearb ? 0.f : cfar) - m_run, r32, hi);
.LBB0_791:
	s_add_i32 s57, s79, 1
	s_add_i32 s101, s49, 0x8000
	s_lshr_b32 s57, s57, 2
	s_lshl_b32 s57, s57, 17
	s_sub_i32 s58, s60, s57
	s_sub_i32 s59, s61, s57
	s_add_i32 s58, s101, s58
	v_lshl_add_u64 v[2:3], v[150:151], 0, s[52:53]
	s_sub_i32 s80, s4, s57
	s_add_i32 m0, s90, s58
	v_lshl_add_u64 v[4:5], v[2:3], 0, s[36:37]
	s_add_i32 s58, s101, s59
	s_sub_i32 s57, s5, s57
	global_load_lds_dwordx4 v[4:5], off
	v_lshl_add_u64 v[4:5], v[148:149], 0, s[52:53]
	s_add_i32 m0, s90, s58
	s_add_i32 s58, s101, s80
	global_load_lds_dwordx4 v[4:5], off
	v_lshl_add_u64 v[2:3], v[2:3], 0, s[24:25]
	s_add_i32 m0, s90, s58
	s_add_i32 s57, s101, s57
	global_load_lds_dwordx4 v[2:3], off
	v_lshl_add_u64 v[2:3], v[146:147], 0, s[52:53]
	s_add_i32 m0, s90, s57
	s_nop 0
	global_load_lds_dwordx4 v[2:3], off
	s_cmp_gt_u32 s94, s67
	s_cbranch_scc1 .LBB0_789
.LBB0_792:
	s_lshr_b32 s57, s94, 2
	s_lshl_b32 s57, s57, 17
	s_add_i32 s100, s94, 1
	s_and_b32 s100, s100, 3
	s_lshl_b32 s100, s100, 15
	s_cmp_le_u32 s48, s88
	s_cselect_b64 vcc, -1, 0
	s_add_i32 s58, s49, 0
	s_waitcnt lgkmcnt(0)
	v_cndmask_b32_e32 v2, 0, v158, vcc
	v_sub_f32_e32 v96, v2, v165
	v_mov_b32_e32 v97, v96
	v_mov_b32_e32 v98, v96
	v_mov_b32_e32 v99, v96
	v_mov_b32_e32 v100, v96
	v_mov_b32_e32 v101, v96
	v_mov_b32_e32 v102, v96
	v_mov_b32_e32 v103, v96
	v_mov_b32_e32 v104, v96
	v_mov_b32_e32 v105, v96
	v_mov_b32_e32 v106, v96
	v_mov_b32_e32 v107, v96
	v_mov_b32_e32 v108, v96
	v_mov_b32_e32 v109, v96
	v_mov_b32_e32 v110, v96
	v_mov_b32_e32 v111, v96
	s_waitcnt lgkmcnt(0)
	s_nop 0
	v_mfma_f32_32x32x16_bf16 v[112:127], v[186:189], v[128:131], v[96:111]
	s_and_b64 vcc, exec, vcc
	v_mfma_f32_32x32x16_bf16 v[96:111], v[190:193], v[128:131], v[96:111]
	v_mfma_f32_32x32x16_bf16 v[112:127], v[202:205], v[132:135], v[112:127]
	v_mfma_f32_32x32x16_bf16 v[96:111], v[206:209], v[132:135], v[96:111]
	v_mfma_f32_32x32x16_bf16 v[112:127], v[210:213], v[136:139], v[112:127]
	v_mfma_f32_32x32x16_bf16 v[96:111], v[214:217], v[136:139], v[96:111]
	v_mfma_f32_32x32x16_bf16 v[112:127], v[218:221], v[140:143], v[112:127]
	v_mfma_f32_32x32x16_bf16 v[96:111], v[222:225], v[140:143], v[96:111]
	s_cbranch_vccnz .LBB0_794
	v_add_u32_e32 v0, 0, v159
	v_add_u32_e32 v2, 0x207fc, v0
	v_add_u32_e32 v4, 0x2087c, v0
	ds_read2_b32 v[2:3], v2 offset1:1
	ds_read2_b32 v[4:5], v4 offset1:1
	v_add_u32_e32 v6, 0x20804, v0
	v_add_u32_e32 v8, 0x20884, v0
	v_add_u32_e32 v10, 0x2081c, v0
	v_add_u32_e32 v12, 0x2089c, v0
	v_add_u32_e32 v14, 0x20824, v0
	v_add_u32_e32 v166, 0x208a4, v0
	v_add_u32_e32 v168, 0x2083c, v0
	v_add_u32_e32 v170, 0x208bc, v0
	v_add_u32_e32 v172, 0x20844, v0
	v_add_u32_e32 v174, 0x208c4, v0
	v_add_u32_e32 v176, 0x2085c, v0
	v_add_u32_e32 v178, 0x208dc, v0
	v_add_u32_e32 v180, 0x20864, v0
	v_add_u32_e32 v0, 0x208e4, v0
	ds_read2_b32 v[6:7], v6 offset1:1
	ds_read2_b32 v[8:9], v8 offset1:1
	ds_read2_b32 v[10:11], v10 offset1:1
	ds_read2_b32 v[12:13], v12 offset1:1
	ds_read2_b32 v[14:15], v14 offset1:1
	ds_read2_b32 v[166:167], v166 offset1:1
	ds_read2_b32 v[168:169], v168 offset1:1
	ds_read2_b32 v[170:171], v170 offset1:1
	ds_read2_b32 v[172:173], v172 offset1:1
	ds_read2_b32 v[174:175], v174 offset1:1
	ds_read2_b32 v[176:177], v176 offset1:1
	ds_read2_b32 v[178:179], v178 offset1:1
	ds_read2_b32 v[180:181], v180 offset1:1
	s_waitcnt lgkmcnt(0)
	v_pk_add_f32 v[112:113], v[112:113], v[2:3]
	ds_read2_b32 v[2:3], v0 offset1:1
	v_pk_add_f32 v[124:125], v[124:125], v[176:177]
	v_pk_add_f32 v[122:123], v[122:123], v[172:173]
	v_pk_add_f32 v[126:127], v[126:127], v[180:181]
	v_pk_add_f32 v[120:121], v[120:121], v[168:169]
	v_pk_add_f32 v[118:119], v[118:119], v[14:15]
	v_pk_add_f32 v[116:117], v[116:117], v[10:11]
	v_pk_add_f32 v[114:115], v[114:115], v[6:7]
	s_waitcnt lgkmcnt(0)
	v_pk_add_f32 v[110:111], v[110:111], v[2:3]
	v_pk_add_f32 v[108:109], v[108:109], v[178:179]
	v_pk_add_f32 v[106:107], v[106:107], v[174:175]
	v_pk_add_f32 v[104:105], v[104:105], v[170:171]
	v_pk_add_f32 v[102:103], v[102:103], v[166:167]
	v_pk_add_f32 v[100:101], v[100:101], v[12:13]
	v_pk_add_f32 v[98:99], v[98:99], v[8:9]
	v_pk_add_f32 v[96:97], v[96:97], v[4:5]

; template <int KS> DI void at_qk(f32x16& p0, f32x16& p1, LAS const unsigned char* Kt, int mapB, const bf16x8 (&qr)[8], float init, int r32, int hi) {
;     ...
;     for (int d0 = 0; d0 < KS; ++d0) { const int cb = mapB + (d0 * 16 + hi * 8) * 2;
;         kb[d0][0] = *(const LAS bf16x8*)(Kt + AT_KSWZ(r32, cb)); kb[d0][1] = *(const LAS bf16x8*)(Kt + AT_KSWZ(32 + r32, cb)); }
;     __builtin_amdgcn_sched_barrier(0);
; #pragma unroll
;     for (int d0 = 0; d0 < KS; ++d0) { p0 = MFMA32(kb[d0][0], qr[d0], p0); p1 = MFMA32(kb[d0][1], qr[d0], p1); }
; }
; DI float at_softmax(f32x16& p0, f32x16& p1, float& m_run, bool first, bool nearb, LAS const float* tabp, int lane) {
;     if (nearb) {
; #pragma unroll
;         for (int i = 0; i < 16; ++i) { p0[i] += tabp[8 * (i >> 2) + (i & 3)]; p1[i] += tabp[32 + 8 * (i >> 2) + (i & 3)]; }
;     }
;     float mx = p0[0];
; #pragma unroll
;     for (int i = 1; i < 16; ++i) mx = fmaxf(mx, p0[i]);
; #pragma unroll
;     for (int i = 0; i < 16; ++i) mx = fmaxf(mx, p1[i]);
;     float alpha = 1.f;
;     if (first || !__all(mx <= AT_THR)) {
;         mx = max_x32(mx, lane);
;         const float dl = first ? mx : fmaxf(mx, 0.f);
;         alpha = first ? 1.f : __builtin_amdgcn_exp2f(-dl); m_run += dl;
; #pragma unroll
;         for (int i = 0; i < 16; ++i) { p0[i] -= dl; p1[i] -= dl; }
;     }
; #pragma unroll
;     for (int i = 0; i < 16; ++i) p0[i] = __builtin_amdgcn_exp2f(p0[i]);
; #pragma unroll
;     for (int i = 0; i < 16; ++i) p1[i] = __builtin_amdgcn_exp2f(p1[i]);
;     return alpha;
; }
; DI bf16x8 at_pack(const f32x16& p, int s8) {
;     u32x4 w; w.x = at_cvtpk(p[s8], p[s8 + 1]); w.y = at_cvtpk(p[s8 + 2], p[s8 + 3]); w.z = at_cvtpk(p[s8 + 4], p[s8 + 5]); w.w = at_cvtpk(p[s8 + 6], p[s8 + 7]);
;     return __builtin_bit_cast(bf16x8, w);
; }
; template <int D0> DI void at_pv_block(f32x16 (&o)[4], int vb, const bf16x8 (&pf)[4]) {
;     const s16x4 l0 = at_tr_read<D0 * 512 + 0 * 4096>(vb), h0 = at_tr_read<D0 * 512 + 0 * 4096 + 2048>(vb), l1 = at_tr_read<D0 * 512 + 1 * 4096>(vb), h1 = at_tr_read<D0 * 512 + 1 * 4096 + 2048>(vb);
;     const s16x4 l2 = at_tr_read<D0 * 512 + 2 * 4096>(vb), h2 = at_tr_read<D0 * 512 + 2 * 4096 + 2048>(vb), l3 = at_tr_read<D0 * 512 + 3 * 4096>(vb), h3 = at_tr_read<D0 * 512 + 3 * 4096 + 2048>(vb);
;     asm volatile("s_waitcnt lgkmcnt(0)" ::: "memory"); __builtin_amdgcn_sched_barrier(0);
.LBB0_801:
	v_subrev_u32_e32 v87, s57, v160
	v_add_u32_e32 v87, s49, v87
	ds_read_b64_tr_b16 v[170:171], v87 offset:0x0
	ds_read_b64_tr_b16 v[172:173], v87 offset:0x800
	ds_read_b64_tr_b16 v[174:175], v87 offset:0x200
	ds_read_b64_tr_b16 v[176:177], v87 offset:0xa00
	ds_read_b64_tr_b16 v[178:179], v87 offset:0x400
	ds_read_b64_tr_b16 v[180:181], v87 offset:0xc00
	ds_read_b64_tr_b16 v[182:183], v87 offset:0x600
	ds_read_b64_tr_b16 v[184:185], v87 offset:0xe00
	v_exp_f32_e32 v112, v112
	v_exp_f32_e32 v113, v113
	v_exp_f32_e32 v114, v114
	v_exp_f32_e32 v115, v115
	v_exp_f32_e32 v116, v116
	v_exp_f32_e32 v117, v117
	v_exp_f32_e32 v118, v118
	v_exp_f32_e32 v119, v119
	v_cvt_pk_bf16_f32 v2, v112, v113
	v_cvt_pk_bf16_f32 v3, v114, v115
	v_cvt_pk_bf16_f32 v4, v116, v117
	v_cvt_pk_bf16_f32 v5, v118, v119
	v_add_f32_e32 v81, v112, v113
	v_add_f32_e32 v82, v114, v115
	v_add_f32_e32 v83, v116, v117
	v_add_f32_e32 v84, v118, v119
	v_add_f32_e32 v81, v81, v82
	v_add_f32_e32 v83, v83, v84
	v_add_f32_e32 v81, v81, v83
	v_add_f32_e32 v80, v80, v81
	s_waitcnt lgkmcnt(0)
	ds_read_b64_tr_b16 v[112:113], v87 offset:0x1000
	ds_read_b64_tr_b16 v[114:115], v87 offset:0x1800
	ds_read_b64_tr_b16 v[116:117], v87 offset:0x1200
	ds_read_b64_tr_b16 v[118:119], v87 offset:0x1a00
	ds_read_b64_tr_b16 v[88:89], v87 offset:0x1400
	ds_read_b64_tr_b16 v[90:91], v87 offset:0x1c00
	ds_read_b64_tr_b16 v[92:93], v87 offset:0x1600
	ds_read_b64_tr_b16 v[94:95], v87 offset:0x1e00
	v_add_u32_e32 v0, s100, v161
	ds_read_b128 v[186:189], v0
	ds_read_b128 v[190:193], v0 offset:8192
	v_mfma_f32_32x32x16_bf16 v[64:79], v[170:173], v[2:5], v[64:79]
	v_exp_f32_e32 v120, v120
	v_exp_f32_e32 v121, v121
	v_mfma_f32_32x32x16_bf16 v[48:63], v[174:177], v[2:5], v[48:63]
	v_exp_f32_e32 v122, v122
	v_exp_f32_e32 v123, v123
	v_mfma_f32_32x32x16_bf16 v[32:47], v[178:181], v[2:5], v[32:47]
	v_exp_f32_e32 v124, v124
	v_exp_f32_e32 v125, v125
	v_mfma_f32_32x32x16_bf16 v[16:31], v[182:185], v[2:5], v[16:31]
	v_exp_f32_e32 v126, v126
	v_exp_f32_e32 v127, v127
	v_cvt_pk_bf16_f32 v6, v120, v121
	v_cvt_pk_bf16_f32 v7, v122, v123
	v_cvt_pk_bf16_f32 v8, v124, v125
	v_cvt_pk_bf16_f32 v9, v126, v127
	v_add_f32_e32 v81, v120, v121
	v_add_f32_e32 v82, v122, v123
	v_add_f32_e32 v83, v124, v125
	v_add_f32_e32 v84, v126, v127
	v_add_f32_e32 v81, v81, v82
	v_add_f32_e32 v83, v83, v84
	v_add_f32_e32 v81, v81, v83
	v_add_f32_e32 v80, v80, v81
	s_waitcnt lgkmcnt(0)
	ds_read_b64_tr_b16 v[170:171], v87 offset:0x2000
	ds_read_b64_tr_b16 v[172:173], v87 offset:0x2800
	ds_read_b64_tr_b16 v[174:175], v87 offset:0x2200
	ds_read_b64_tr_b16 v[176:177], v87 offset:0x2a00
	ds_read_b64_tr_b16 v[178:179], v87 offset:0x2400
	ds_read_b64_tr_b16 v[180:181], v87 offset:0x2c00
	ds_read_b64_tr_b16 v[182:183], v87 offset:0x2600
	ds_read_b64_tr_b16 v[184:185], v87 offset:0x2e00
	v_add_u32_e32 v0, s100, v162
	ds_read_b128 v[202:205], v0
	ds_read_b128 v[206:209], v0 offset:8192
	v_mfma_f32_32x32x16_bf16 v[64:79], v[112:115], v[6:9], v[64:79]
	v_exp_f32_e32 v96, v96
	v_exp_f32_e32 v97, v97
	v_mfma_f32_32x32x16_bf16 v[48:63], v[116:119], v[6:9], v[48:63]
	v_exp_f32_e32 v98, v98
	v_exp_f32_e32 v99, v99
	v_mfma_f32_32x32x16_bf16 v[32:47], v[88:91], v[6:9], v[32:47]
	v_exp_f32_e32 v100, v100
	v_exp_f32_e32 v101, v101
	v_mfma_f32_32x32x16_bf16 v[16:31], v[92:95], v[6:9], v[16:31]
	v_exp_f32_e32 v102, v102
	v_exp_f32_e32 v103, v103
	v_cvt_pk_bf16_f32 v10, v96, v97
	v_cvt_pk_bf16_f32 v11, v98, v99
	v_cvt_pk_bf16_f32 v12, v100, v101
	v_cvt_pk_bf16_f32 v13, v102, v103
	v_add_f32_e32 v81, v96, v97
	v_add_f32_e32 v82, v98, v99
	v_add_f32_e32 v83, v100, v101
	v_add_f32_e32 v84, v102, v103
	v_add_f32_e32 v81, v81, v82
	v_add_f32_e32 v83, v83, v84
	v_add_f32_e32 v81, v81, v83
	v_add_f32_e32 v80, v80, v81
	s_waitcnt lgkmcnt(0)
	ds_read_b64_tr_b16 v[112:113], v87 offset:0x3000
	ds_read_b64_tr_b16 v[114:115], v87 offset:0x3800
	ds_read_b64_tr_b16 v[116:117], v87 offset:0x3200
	ds_read_b64_tr_b16 v[118:119], v87 offset:0x3a00
	ds_read_b64_tr_b16 v[88:89], v87 offset:0x3400
	ds_read_b64_tr_b16 v[90:91], v87 offset:0x3c00
	ds_read_b64_tr_b16 v[92:93], v87 offset:0x3600
	ds_read_b64_tr_b16 v[94:95], v87 offset:0x3e00
	v_add_u32_e32 v0, s100, v163
	ds_read_b128 v[210:213], v0
	ds_read_b128 v[214:217], v0 offset:8192
	v_mfma_f32_32x32x16_bf16 v[64:79], v[170:173], v[10:13], v[64:79]
	v_exp_f32_e32 v104, v104
	v_exp_f32_e32 v105, v105
	v_mfma_f32_32x32x16_bf16 v[48:63], v[174:177], v[10:13], v[48:63]
	v_exp_f32_e32 v106, v106
	v_exp_f32_e32 v107, v107
	v_mfma_f32_32x32x16_bf16 v[32:47], v[178:181], v[10:13], v[32:47]
	v_exp_f32_e32 v108, v108
	v_exp_f32_e32 v109, v109
	v_mfma_f32_32x32x16_bf16 v[16:31], v[182:185], v[10:13], v[16:31]
	v_exp_f32_e32 v110, v110
	v_exp_f32_e32 v111, v111
	v_cvt_pk_bf16_f32 v166, v104, v105
	v_cvt_pk_bf16_f32 v167, v106, v107
	v_cvt_pk_bf16_f32 v168, v108, v109
	v_cvt_pk_bf16_f32 v169, v110, v111
	v_add_f32_e32 v81, v104, v105
	v_add_f32_e32 v82, v106, v107
	v_add_f32_e32 v83, v108, v109
	v_add_f32_e32 v84, v110, v111
	v_add_f32_e32 v81, v81, v82
	v_add_f32_e32 v83, v83, v84
	v_add_f32_e32 v81, v81, v83
	v_add_f32_e32 v80, v80, v81
	s_waitcnt lgkmcnt(0)
	v_add_u32_e32 v0, s100, v164
	ds_read_b128 v[218:221], v0
	ds_read_b128 v[222:225], v0 offset:8192
	v_mfma_f32_32x32x16_bf16 v[64:79], v[112:115], v[166:169], v[64:79]
	v_mfma_f32_32x32x16_bf16 v[48:63], v[116:119], v[166:169], v[48:63]
	v_mfma_f32_32x32x16_bf16 v[32:47], v[88:91], v[166:169], v[32:47]
	v_mfma_f32_32x32x16_bf16 v[16:31], v[92:95], v[166:169], v[16:31]
	s_mov_b64 s[38:39], 0
	s_mov_b64 s[58:59], -1
	s_and_b64 vcc, exec, s[40:41]
	s_cbranch_vccz .LBB0_790

; #define AT_BAR() asm volatile("s_waitcnt vmcnt(0) lgkmcnt(0)\n\ts_barrier" ::: "memory")
; DI int at_v_rd_base(int lane) { return ((lane & 3) << 3) | (((lane >> 2) & 3) << 6) | (((lane >> 4) & 1) << 5) | (((lane >> 5) & 1) << 8); }
; DI void attn_unit_diff(const Ctx& C, int l, int b, int h, int j) {
;     ...
;     AT_BAR();
;     unsigned lb0, lb1;
;     { const int kv = wid >> 2;
;       if (kv == 0) { const int rl = lane >> 4, cp = lane & 15; lb0 = (unsigned)(rl * (INW * 2) + ((cp ^ (rl & 7)) * 16)); lb1 = (unsigned)(rl * (INW * 2) + ((cp ^ ((4 + rl) & 7)) * 16)); }
;       else { lb0 = (unsigned)(((lane & 31) >> 2) * (INW * 2) + ((lane >> 5) * 32 + (lane & 3) * 8) * 2); lb1 = lb0; } }
;     at_stage1(C.lds, projb, kcolB, vcolB, 0, 0, wid, lb0, lb1);
;     at_stage1(C.lds, projb, kcolB, vcolB, 1, 1, wid, lb0, lb1);
;     __builtin_amdgcn_sched_barrier(0);
;     bf16x8 qr[8];
;     { const bf16_t* qp = proj + (rowb + qpos) * INW + qcol + 8 * hi;
; #pragma unroll
;       for (int s = 0; s < KS; ++s) qr[s] = *(const bf16x8*)(qp + 16 * s); }
;     for (int i = wid * 64 + lane; i < TABB_N; i += NTHREADS) tabl[i] = tabg[i];
;     f32x16 o[4], ol = {}; float m_run = 0.f; bool first = true;
; #pragma unroll
;     for (int d0 = 0; d0 < 4; ++d0) o[d0] = f32x16{};
;     const bf16x8 ones = {16256, 16256, 16256, 16256, 16256, 16256, 16256, 16256};
;     asm volatile("s_waitcnt vmcnt(0) lgkmcnt(0)\n\ts_barrier" ::: "memory");
;     const float cfar = tabl[0];
;     const int vrd = at_v_rd_base(lane);
;     for (int sd = 0; sd < nt; ++sd) {
;         const int slot = sd % 3;
;         const bool staged = sd + 2 < nt;
;         if (staged) at_stage1(C.lds, projb, kcolB, vcolB, sd + 2, (sd + 2) % 3, wid, lb0, lb1);
.LBB0_828:
	s_or_b64 exec, exec, s[58:59]
	s_and_b32 s11, s22, 15
	s_waitcnt vmcnt(0) lgkmcnt(0)
	s_barrier
	v_mov_b32_e32 v4, s50
	s_lshl_b32 s6, s6, 1
	v_readlane_b32 s7, v252, 22
	s_lshl_b32 s31, s11, 7
	s_lshl_b32 s11, s11, 16
	s_waitcnt lgkmcnt(0)
	ds_read_b32 v158, v4
	v_and_b32_e32 v4, 24, v8
	v_and_b32_e32 v7, 0x100, v8
	v_lshlrev_b32_e32 v8, 4, v156
	v_readlane_b32 s15, v252, 26
	v_readlane_b32 s35, v252, 23
	v_mov_b32_e32 v3, v1
	s_or_b32 s7, s6, s7
	s_add_i32 s11, s11, 0x10000
	v_lshlrev_b32_e32 v145, 4, v154
	v_add_u32_e32 v9, s15, v8
	v_lshlrev_b32_e32 v11, 4, v155
	v_lshlrev_b32_e32 v15, 2, v154
	s_add_i32 s16, s55, 0xfffffe90
	s_or_b32 s31, s35, s31
	s_add_i32 s52, s48, s28
	v_and_b32_e32 v5, 0xc0, v145
	v_lshlrev_b32_e32 v6, 1, v154
	v_lshlrev_b32_e32 v10, 8, v155
	v_and_b32_e32 v11, 0x70, v11
	v_add_u32_e32 v14, 0x60, v9
	v_xor_b32_e32 v157, 0x80, v15
	v_add_lshl_u32 v15, s31, v155, 2
	v_lshl_add_u64 v[2:3], s[42:43], 0, v[2:3]
	s_add_u32 s42, s96, s42
	v_and_b32_e32 v6, 32, v6
	v_add_u32_e32 v12, 32, v9
	v_add_u32_e32 v13, 64, v9
	v_sub_u32_e32 v159, v8, v15
	v_add3_u32 v5, v7, s91, v5
	v_xad_u32 v164, v14, v11, v10
	s_addc_u32 s43, s89, s43
	v_mov_b32_e32 v14, v1
	v_mov_b32_e32 v15, v1
	v_add3_u32 v160, v5, v6, v4
	v_xad_u32 v161, v9, v11, v10
	v_xad_u32 v162, v12, v11, v10
	v_xad_u32 v163, v13, v11, v10
	v_lshl_add_u64 v[146:147], s[70:71], 0, v[2:3]
	v_lshl_add_u64 v[148:149], s[72:73], 0, v[2:3]
	v_lshl_add_u64 v[150:151], s[42:43], 0, v[0:1]
	v_mov_b32_e32 v0, v1
	v_mov_b32_e32 v2, v1
	v_mov_b32_e32 v3, v1
	v_mov_b32_e32 v4, v1
	v_mov_b32_e32 v5, v1
	v_mov_b32_e32 v6, v1
	v_mov_b32_e32 v7, v1
	v_mov_b32_e32 v8, v1
	v_mov_b32_e32 v9, v1
	v_mov_b32_e32 v10, v1
	v_mov_b32_e32 v11, v1
	v_mov_b32_e32 v12, v1
	v_mov_b32_e32 v13, v1
	v_mov_b64_e32 v[78:79], v[14:15]
	v_mov_b64_e32 v[62:63], v[14:15]
	v_mov_b64_e32 v[46:47], v[14:15]
	v_mov_b64_e32 v[30:31], v[14:15]
	v_mov_b64_e32 v[94:95], v[14:15]
	s_mov_b32 s15, 2
	s_mov_b32 s28, 0
	v_mov_b32_e32 v165, 0
	s_mov_b64 s[42:43], -1
	s_mov_b32 s31, 0
	v_mov_b64_e32 v[76:77], v[12:13]
	v_mov_b64_e32 v[74:75], v[10:11]
	v_mov_b64_e32 v[72:73], v[8:9]
	v_mov_b64_e32 v[70:71], v[6:7]
	v_mov_b64_e32 v[68:69], v[4:5]
	v_mov_b64_e32 v[66:67], v[2:3]
	v_mov_b64_e32 v[64:65], v[0:1]
	v_mov_b64_e32 v[60:61], v[12:13]
	v_mov_b64_e32 v[58:59], v[10:11]
	v_mov_b64_e32 v[56:57], v[8:9]
	v_mov_b64_e32 v[54:55], v[6:7]
	v_mov_b64_e32 v[52:53], v[4:5]
	v_mov_b64_e32 v[50:51], v[2:3]
	v_mov_b64_e32 v[48:49], v[0:1]
	v_mov_b64_e32 v[44:45], v[12:13]
	v_mov_b64_e32 v[42:43], v[10:11]
	v_mov_b64_e32 v[40:41], v[8:9]
	v_mov_b64_e32 v[38:39], v[6:7]
	v_mov_b64_e32 v[36:37], v[4:5]
	v_mov_b64_e32 v[34:35], v[2:3]
	v_mov_b64_e32 v[32:33], v[0:1]
	v_mov_b64_e32 v[28:29], v[12:13]
	v_mov_b64_e32 v[26:27], v[10:11]
	v_mov_b64_e32 v[24:25], v[8:9]
	v_mov_b64_e32 v[22:23], v[6:7]
	v_mov_b64_e32 v[20:21], v[4:5]
	v_mov_b64_e32 v[18:19], v[2:3]
	v_mov_b64_e32 v[16:17], v[0:1]
	v_mov_b64_e32 v[92:93], v[12:13]
	v_mov_b64_e32 v[90:91], v[10:11]
	v_mov_b64_e32 v[88:89], v[8:9]
	v_mov_b64_e32 v[86:87], v[6:7]
	v_mov_b64_e32 v[84:85], v[4:5]
	v_mov_b64_e32 v[82:83], v[2:3]
	v_mov_b64_e32 v[80:81], v[0:1]
	s_mov_b32 s35, 0
	s_waitcnt vmcnt(0)
	s_mul_hi_u32 s48, s15, 0xaaaaaaab
	s_lshr_b32 s48, s48, 1
	s_mul_i32 s48, s48, 0x18000
	s_sub_i32 s49, s60, s48
	s_sub_i32 s57, s61, s48
	s_add_i32 s49, s31, s49
	v_lshl_add_u64 v[2:3], v[150:151], 0, s[52:53]
	s_sub_i32 s58, s4, s48
	s_add_i32 m0, s90, s49
	v_lshl_add_u64 v[4:5], v[2:3], 0, s[36:37]
	s_add_i32 s49, s31, s57
	s_sub_i32 s48, s5, s48
	global_load_lds_dwordx4 v[4:5], off
	v_lshl_add_u64 v[4:5], v[148:149], 0, s[52:53]
	s_add_i32 m0, s90, s49
	s_add_i32 s49, s31, s58
	global_load_lds_dwordx4 v[4:5], off
	v_lshl_add_u64 v[2:3], v[2:3], 0, s[24:25]
	s_add_i32 m0, s90, s49
	s_add_i32 s48, s31, s48
	global_load_lds_dwordx4 v[2:3], off
	v_lshl_add_u64 v[2:3], v[146:147], 0, s[52:53]
	s_add_i32 m0, s90, s48
	s_nop 0
	global_load_lds_dwordx4 v[2:3], off
	v_lshl_add_u64 v[146:147], v[146:147], 0, s[68:69]
	v_lshl_add_u64 v[148:149], v[148:149], 0, s[68:69]
	v_lshl_add_u64 v[150:151], v[150:151], 0, s[68:69]
	ds_read_b128 v[186:189], v161
	ds_read_b128 v[190:193], v161 offset:8192
	ds_read_b128 v[202:205], v162
	ds_read_b128 v[206:209], v162 offset:8192
	ds_read_b128 v[210:213], v163
	ds_read_b128 v[214:217], v163 offset:8192
	ds_read_b128 v[218:221], v164
	ds_read_b128 v[222:225], v164 offset:8192
	s_branch .LBB0_830

; DI void attn_unit_diff(const Ctx& C, int l, int b, int h, int j) {
;     ...
;     for (int sd = 0; sd < nt; ++sd) {
;         const int slot = sd % 3;
;         const bool staged = sd + 2 < nt;
;         if (staged) at_stage1(C.lds, projb, kcolB, vcolB, sd + 2, (sd + 2) % 3, wid, lb0, lb1);
;         if (sd <= cw) {
.LBB0_830:
	s_add_i32 s101, s35, 1
	s_cmp_ge_u32 s101, s6
	s_cselect_b64 s[76:77], -1, 0
	s_and_b64 vcc, exec, s[76:77]
	s_cbranch_vccz .LBB0_834
	s_cmp_gt_u32 s35, s7
	s_cbranch_scc0 .LBB0_835

; #define LAS __attribute__((address_space(3)))
; #define MFMA32(a, b, c) __builtin_amdgcn_mfma_f32_32x32x16_bf16((a), (b), (c), 0, 0, 0)
;     __device__ __forceinline__ void init(const void* A_, const void* B_, int lda_, int ldb_, int M, unsigned mask_, int G_, int c_) { A = (const char*)A_; B = (const char*)B_; lda = lda_; ldb = ldb_; nM = M / BM; mask = mask_; nN = __builtin_popcount(mask_); nwg = nM * nN; G = G_; c = c_; }
;     __device__ __forceinline__ void init(f32x4 (&acc)[2][2][4][2], const Unit& u, int wr, int wc, int fr, int fq) const { u32x4 old[2][4][2]; init_load(old, u, wr, wc, fr, fq); init_finish(acc, old); }
; template <int KS> DI void at_qk(f32x16& p0, f32x16& p1, LAS const unsigned char* Kt, int mapB, const bf16x8 (&qr)[8], float init, int r32, int hi) {
; #pragma unroll
;     for (int i = 0; i < 16; ++i) { p0[i] = init; p1[i] = init; }
;     bf16x8 kb[KS][2];
; #pragma unroll
;     for (int d0 = 0; d0 < KS; ++d0) { const int cb = mapB + (d0 * 16 + hi * 8) * 2;
;         kb[d0][0] = *(const LAS bf16x8*)(Kt + AT_KSWZ(r32, cb)); kb[d0][1] = *(const LAS bf16x8*)(Kt + AT_KSWZ(32 + r32, cb)); }
;     __builtin_amdgcn_sched_barrier(0);
; #pragma unroll
;     for (int d0 = 0; d0 < KS; ++d0) { p0 = MFMA32(kb[d0][0], qr[d0], p0); p1 = MFMA32(kb[d0][1], qr[d0], p1); }
; }
; DI void attn_unit_diff(const Ctx& C, int l, int b, int h, int j) {
;     ...
;         if (staged) at_stage1(C.lds, projb, kcolB, vcolB, sd + 2, (sd + 2) % 3, wid, lb0, lb1);
;         if (sd <= cw) {
;             LAS const unsigned char* Kt = C.lds + slot * 32768;
;             const int vb = (int)(size_t)(Kt + 16384) + vrd;
;             const bool nearb = (sd * 64 + 63 - q0w) > -305;
;             LAS const float* tabp = tabl + (sd * 64 - qpos + TABB_OFF + 4 * hi);
;             f32x16 p0, p1;
;             at_qk<KS>(p0, p1, Kt, g * 128, qr, (nearb ? 0.f : cfar) - m_run, r32, hi);
.LBB0_834:
	s_add_i32 s48, s15, 1
	s_add_i32 s101, s31, 0x8000
	s_lshr_b32 s48, s48, 2
	s_lshl_b32 s48, s48, 17
	s_sub_i32 s49, s60, s48
	s_sub_i32 s57, s61, s48
	s_add_i32 s49, s101, s49
	v_lshl_add_u64 v[2:3], v[150:151], 0, s[52:53]
	s_sub_i32 s58, s4, s48
	s_add_i32 m0, s90, s49
	v_lshl_add_u64 v[4:5], v[2:3], 0, s[36:37]
	s_add_i32 s49, s101, s57
	s_sub_i32 s48, s5, s48
	global_load_lds_dwordx4 v[4:5], off
	v_lshl_add_u64 v[4:5], v[148:149], 0, s[52:53]
	s_add_i32 m0, s90, s49
	s_add_i32 s49, s101, s58
	global_load_lds_dwordx4 v[4:5], off
	v_lshl_add_u64 v[2:3], v[2:3], 0, s[24:25]
	s_add_i32 m0, s90, s49
	s_add_i32 s48, s101, s48
	global_load_lds_dwordx4 v[2:3], off
	v_lshl_add_u64 v[2:3], v[146:147], 0, s[52:53]
	s_add_i32 m0, s90, s48
	s_nop 0
	global_load_lds_dwordx4 v[2:3], off
	s_cmp_gt_u32 s35, s7
	s_cbranch_scc1 .LBB0_832
.LBB0_835:
	s_lshr_b32 s48, s35, 2
	s_lshl_b32 s48, s48, 17
	s_add_i32 s100, s35, 1
	s_and_b32 s100, s100, 3
	s_lshl_b32 s100, s100, 15
	s_cmp_le_i32 s28, s16
	s_cselect_b64 vcc, -1, 0
	s_add_i32 s49, s31, 0
	s_waitcnt lgkmcnt(0)
	v_cndmask_b32_e32 v2, 0, v158, vcc
	v_sub_f32_e32 v96, v2, v165
	v_mov_b32_e32 v97, v96
	v_mov_b32_e32 v98, v96
	v_mov_b32_e32 v99, v96
	v_mov_b32_e32 v100, v96
	v_mov_b32_e32 v101, v96
	v_mov_b32_e32 v102, v96
	v_mov_b32_e32 v103, v96
	v_mov_b32_e32 v104, v96
	v_mov_b32_e32 v105, v96
	v_mov_b32_e32 v106, v96
	v_mov_b32_e32 v107, v96
	v_mov_b32_e32 v108, v96
	v_mov_b32_e32 v109, v96
	v_mov_b32_e32 v110, v96
	v_mov_b32_e32 v111, v96
	s_waitcnt lgkmcnt(0)
	s_nop 0
	v_mfma_f32_32x32x16_bf16 v[112:127], v[186:189], v[128:131], v[96:111]
	s_and_b64 vcc, exec, vcc
	v_mfma_f32_32x32x16_bf16 v[96:111], v[190:193], v[128:131], v[96:111]
	v_mfma_f32_32x32x16_bf16 v[112:127], v[202:205], v[132:135], v[112:127]
	v_mfma_f32_32x32x16_bf16 v[96:111], v[206:209], v[132:135], v[96:111]
	v_mfma_f32_32x32x16_bf16 v[112:127], v[210:213], v[136:139], v[112:127]
	v_mfma_f32_32x32x16_bf16 v[96:111], v[214:217], v[136:139], v[96:111]
	v_mfma_f32_32x32x16_bf16 v[112:127], v[218:221], v[140:143], v[112:127]
	v_mfma_f32_32x32x16_bf16 v[96:111], v[222:225], v[140:143], v[96:111]
	s_cbranch_vccnz .LBB0_837
	v_add_u32_e32 v0, 0, v159
	v_add_u32_e32 v2, 0x207fc, v0
	v_add_u32_e32 v4, 0x2087c, v0
	ds_read2_b32 v[2:3], v2 offset1:1
	ds_read2_b32 v[4:5], v4 offset1:1
	v_add_u32_e32 v6, 0x20804, v0
	v_add_u32_e32 v8, 0x20884, v0
	v_add_u32_e32 v10, 0x2081c, v0
	v_add_u32_e32 v12, 0x2089c, v0
	v_add_u32_e32 v14, 0x20824, v0
	v_add_u32_e32 v166, 0x208a4, v0
	v_add_u32_e32 v168, 0x2083c, v0
	v_add_u32_e32 v170, 0x208bc, v0
	v_add_u32_e32 v172, 0x20844, v0
	v_add_u32_e32 v174, 0x208c4, v0
	v_add_u32_e32 v176, 0x2085c, v0
	v_add_u32_e32 v178, 0x208dc, v0
	v_add_u32_e32 v180, 0x20864, v0
	v_add_u32_e32 v0, 0x208e4, v0
	ds_read2_b32 v[6:7], v6 offset1:1
	ds_read2_b32 v[8:9], v8 offset1:1
	ds_read2_b32 v[10:11], v10 offset1:1
	ds_read2_b32 v[12:13], v12 offset1:1
	ds_read2_b32 v[14:15], v14 offset1:1
	ds_read2_b32 v[166:167], v166 offset1:1
	ds_read2_b32 v[168:169], v168 offset1:1
	ds_read2_b32 v[170:171], v170 offset1:1
	ds_read2_b32 v[172:173], v172 offset1:1
	ds_read2_b32 v[174:175], v174 offset1:1
	ds_read2_b32 v[176:177], v176 offset1:1
	ds_read2_b32 v[178:179], v178 offset1:1
	ds_read2_b32 v[180:181], v180 offset1:1
	s_waitcnt lgkmcnt(0)
	v_pk_add_f32 v[112:113], v[112:113], v[2:3]
	ds_read2_b32 v[2:3], v0 offset1:1
	v_pk_add_f32 v[124:125], v[124:125], v[176:177]
	v_pk_add_f32 v[122:123], v[122:123], v[172:173]
	v_pk_add_f32 v[126:127], v[126:127], v[180:181]
	v_pk_add_f32 v[120:121], v[120:121], v[168:169]
	v_pk_add_f32 v[118:119], v[118:119], v[14:15]
	v_pk_add_f32 v[116:117], v[116:117], v[10:11]
	v_pk_add_f32 v[114:115], v[114:115], v[6:7]
	s_waitcnt lgkmcnt(0)
	v_pk_add_f32 v[110:111], v[110:111], v[2:3]
	v_pk_add_f32 v[108:109], v[108:109], v[178:179]
	v_pk_add_f32 v[106:107], v[106:107], v[174:175]
	v_pk_add_f32 v[104:105], v[104:105], v[170:171]
	v_pk_add_f32 v[102:103], v[102:103], v[166:167]
	v_pk_add_f32 v[100:101], v[100:101], v[12:13]
	v_pk_add_f32 v[98:99], v[98:99], v[8:9]
	v_pk_add_f32 v[96:97], v[96:97], v[4:5]

; template <int KS> DI void at_qk(f32x16& p0, f32x16& p1, LAS const unsigned char* Kt, int mapB, const bf16x8 (&qr)[8], float init, int r32, int hi) {
;     ...
;     for (int d0 = 0; d0 < KS; ++d0) { const int cb = mapB + (d0 * 16 + hi * 8) * 2;
;         kb[d0][0] = *(const LAS bf16x8*)(Kt + AT_KSWZ(r32, cb)); kb[d0][1] = *(const LAS bf16x8*)(Kt + AT_KSWZ(32 + r32, cb)); }
;     __builtin_amdgcn_sched_barrier(0);
; #pragma unroll
;     for (int d0 = 0; d0 < KS; ++d0) { p0 = MFMA32(kb[d0][0], qr[d0], p0); p1 = MFMA32(kb[d0][1], qr[d0], p1); }
; }
; DI float at_softmax(f32x16& p0, f32x16& p1, float& m_run, bool first, bool nearb, LAS const float* tabp, int lane) {
;     if (nearb) {
; #pragma unroll
;         for (int i = 0; i < 16; ++i) { p0[i] += tabp[8 * (i >> 2) + (i & 3)]; p1[i] += tabp[32 + 8 * (i >> 2) + (i & 3)]; }
;     }
;     float mx = p0[0];
; #pragma unroll
;     for (int i = 1; i < 16; ++i) mx = fmaxf(mx, p0[i]);
; #pragma unroll
;     for (int i = 0; i < 16; ++i) mx = fmaxf(mx, p1[i]);
;     float alpha = 1.f;
;     if (first || !__all(mx <= AT_THR)) {
;         mx = max_x32(mx, lane);
;         const float dl = first ? mx : fmaxf(mx, 0.f);
;         alpha = first ? 1.f : __builtin_amdgcn_exp2f(-dl); m_run += dl;
; #pragma unroll
;         for (int i = 0; i < 16; ++i) { p0[i] -= dl; p1[i] -= dl; }
;     }
; #pragma unroll
;     for (int i = 0; i < 16; ++i) p0[i] = __builtin_amdgcn_exp2f(p0[i]);
; #pragma unroll
;     for (int i = 0; i < 16; ++i) p1[i] = __builtin_amdgcn_exp2f(p1[i]);
;     return alpha;
; }
; DI bf16x8 at_pack(const f32x16& p, int s8) {
;     u32x4 w; w.x = at_cvtpk(p[s8], p[s8 + 1]); w.y = at_cvtpk(p[s8 + 2], p[s8 + 3]); w.z = at_cvtpk(p[s8 + 4], p[s8 + 5]); w.w = at_cvtpk(p[s8 + 6], p[s8 + 7]);
;     return __builtin_bit_cast(bf16x8, w);
; }
; template <int D0> DI void at_pv_block(f32x16 (&o)[4], int vb, const bf16x8 (&pf)[4]) {
;     const s16x4 l0 = at_tr_read<D0 * 512 + 0 * 4096>(vb), h0 = at_tr_read<D0 * 512 + 0 * 4096 + 2048>(vb), l1 = at_tr_read<D0 * 512 + 1 * 4096>(vb), h1 = at_tr_read<D0 * 512 + 1 * 4096 + 2048>(vb);
;     const s16x4 l2 = at_tr_read<D0 * 512 + 2 * 4096>(vb), h2 = at_tr_read<D0 * 512 + 2 * 4096 + 2048>(vb), l3 = at_tr_read<D0 * 512 + 3 * 4096>(vb), h3 = at_tr_read<D0 * 512 + 3 * 4096 + 2048>(vb);
;     asm volatile("s_waitcnt lgkmcnt(0)" ::: "memory"); __builtin_amdgcn_sched_barrier(0);
.LBB0_844:
	v_subrev_u32_e32 v87, s48, v160
	v_add_u32_e32 v87, s31, v87
	ds_read_b64_tr_b16 v[170:171], v87 offset:0x0
	ds_read_b64_tr_b16 v[172:173], v87 offset:0x800
	ds_read_b64_tr_b16 v[174:175], v87 offset:0x200
	ds_read_b64_tr_b16 v[176:177], v87 offset:0xa00
	ds_read_b64_tr_b16 v[178:179], v87 offset:0x400
	ds_read_b64_tr_b16 v[180:181], v87 offset:0xc00
	ds_read_b64_tr_b16 v[182:183], v87 offset:0x600
	ds_read_b64_tr_b16 v[184:185], v87 offset:0xe00
	v_exp_f32_e32 v112, v112
	v_exp_f32_e32 v113, v113
	v_exp_f32_e32 v114, v114
	v_exp_f32_e32 v115, v115
	v_exp_f32_e32 v116, v116
	v_exp_f32_e32 v117, v117
	v_exp_f32_e32 v118, v118
	v_exp_f32_e32 v119, v119
	v_cvt_pk_bf16_f32 v2, v112, v113
	v_cvt_pk_bf16_f32 v3, v114, v115
	v_cvt_pk_bf16_f32 v4, v116, v117
	v_cvt_pk_bf16_f32 v5, v118, v119
	v_add_f32_e32 v81, v112, v113
	v_add_f32_e32 v82, v114, v115
	v_add_f32_e32 v83, v116, v117
	v_add_f32_e32 v84, v118, v119
	v_add_f32_e32 v81, v81, v82
	v_add_f32_e32 v83, v83, v84
	v_add_f32_e32 v81, v81, v83
	v_add_f32_e32 v80, v80, v81
	s_waitcnt lgkmcnt(0)
	ds_read_b64_tr_b16 v[112:113], v87 offset:0x1000
	ds_read_b64_tr_b16 v[114:115], v87 offset:0x1800
	ds_read_b64_tr_b16 v[116:117], v87 offset:0x1200
	ds_read_b64_tr_b16 v[118:119], v87 offset:0x1a00
	ds_read_b64_tr_b16 v[88:89], v87 offset:0x1400
	ds_read_b64_tr_b16 v[90:91], v87 offset:0x1c00
	ds_read_b64_tr_b16 v[92:93], v87 offset:0x1600
	ds_read_b64_tr_b16 v[94:95], v87 offset:0x1e00
	v_add_u32_e32 v0, s100, v161
	ds_read_b128 v[186:189], v0
	ds_read_b128 v[190:193], v0 offset:8192
	v_mfma_f32_32x32x16_bf16 v[64:79], v[170:173], v[2:5], v[64:79]
	v_exp_f32_e32 v120, v120
	v_exp_f32_e32 v121, v121
	v_mfma_f32_32x32x16_bf16 v[48:63], v[174:177], v[2:5], v[48:63]
	v_exp_f32_e32 v122, v122
	v_exp_f32_e32 v123, v123
	v_mfma_f32_32x32x16_bf16 v[32:47], v[178:181], v[2:5], v[32:47]
	v_exp_f32_e32 v124, v124
	v_exp_f32_e32 v125, v125
	v_mfma_f32_32x32x16_bf16 v[16:31], v[182:185], v[2:5], v[16:31]
	v_exp_f32_e32 v126, v126
	v_exp_f32_e32 v127, v127
	v_cvt_pk_bf16_f32 v6, v120, v121
	v_cvt_pk_bf16_f32 v7, v122, v123
	v_cvt_pk_bf16_f32 v8, v124, v125
	v_cvt_pk_bf16_f32 v9, v126, v127
	v_add_f32_e32 v81, v120, v121
	v_add_f32_e32 v82, v122, v123
	v_add_f32_e32 v83, v124, v125
	v_add_f32_e32 v84, v126, v127
	v_add_f32_e32 v81, v81, v82
	v_add_f32_e32 v83, v83, v84
	v_add_f32_e32 v81, v81, v83
	v_add_f32_e32 v80, v80, v81
	s_waitcnt lgkmcnt(0)
	ds_read_b64_tr_b16 v[170:171], v87 offset:0x2000
	ds_read_b64_tr_b16 v[172:173], v87 offset:0x2800
	ds_read_b64_tr_b16 v[174:175], v87 offset:0x2200
	ds_read_b64_tr_b16 v[176:177], v87 offset:0x2a00
	ds_read_b64_tr_b16 v[178:179], v87 offset:0x2400
	ds_read_b64_tr_b16 v[180:181], v87 offset:0x2c00
	ds_read_b64_tr_b16 v[182:183], v87 offset:0x2600
	ds_read_b64_tr_b16 v[184:185], v87 offset:0x2e00
	v_add_u32_e32 v0, s100, v162
	ds_read_b128 v[202:205], v0
	ds_read_b128 v[206:209], v0 offset:8192
	v_mfma_f32_32x32x16_bf16 v[64:79], v[112:115], v[6:9], v[64:79]
	v_exp_f32_e32 v96, v96
	v_exp_f32_e32 v97, v97
	v_mfma_f32_32x32x16_bf16 v[48:63], v[116:119], v[6:9], v[48:63]
	v_exp_f32_e32 v98, v98
	v_exp_f32_e32 v99, v99
	v_mfma_f32_32x32x16_bf16 v[32:47], v[88:91], v[6:9], v[32:47]
	v_exp_f32_e32 v100, v100
	v_exp_f32_e32 v101, v101
	v_mfma_f32_32x32x16_bf16 v[16:31], v[92:95], v[6:9], v[16:31]
	v_exp_f32_e32 v102, v102
	v_exp_f32_e32 v103, v103
	v_cvt_pk_bf16_f32 v10, v96, v97
	v_cvt_pk_bf16_f32 v11, v98, v99
	v_cvt_pk_bf16_f32 v12, v100, v101
	v_cvt_pk_bf16_f32 v13, v102, v103
	v_add_f32_e32 v81, v96, v97
	v_add_f32_e32 v82, v98, v99
	v_add_f32_e32 v83, v100, v101
	v_add_f32_e32 v84, v102, v103
	v_add_f32_e32 v81, v81, v82
	v_add_f32_e32 v83, v83, v84
	v_add_f32_e32 v81, v81, v83
	v_add_f32_e32 v80, v80, v81
	s_waitcnt lgkmcnt(0)
	ds_read_b64_tr_b16 v[112:113], v87 offset:0x3000
	ds_read_b64_tr_b16 v[114:115], v87 offset:0x3800
	ds_read_b64_tr_b16 v[116:117], v87 offset:0x3200
	ds_read_b64_tr_b16 v[118:119], v87 offset:0x3a00
	ds_read_b64_tr_b16 v[88:89], v87 offset:0x3400
	ds_read_b64_tr_b16 v[90:91], v87 offset:0x3c00
	ds_read_b64_tr_b16 v[92:93], v87 offset:0x3600
	ds_read_b64_tr_b16 v[94:95], v87 offset:0x3e00
	v_add_u32_e32 v0, s100, v163
	ds_read_b128 v[210:213], v0
	ds_read_b128 v[214:217], v0 offset:8192
	v_mfma_f32_32x32x16_bf16 v[64:79], v[170:173], v[10:13], v[64:79]
	v_exp_f32_e32 v104, v104
	v_exp_f32_e32 v105, v105
	v_mfma_f32_32x32x16_bf16 v[48:63], v[174:177], v[10:13], v[48:63]
	v_exp_f32_e32 v106, v106
	v_exp_f32_e32 v107, v107
	v_mfma_f32_32x32x16_bf16 v[32:47], v[178:181], v[10:13], v[32:47]
	v_exp_f32_e32 v108, v108
	v_exp_f32_e32 v109, v109
	v_mfma_f32_32x32x16_bf16 v[16:31], v[182:185], v[10:13], v[16:31]
	v_exp_f32_e32 v110, v110
	v_exp_f32_e32 v111, v111
	v_cvt_pk_bf16_f32 v166, v104, v105
	v_cvt_pk_bf16_f32 v167, v106, v107
	v_cvt_pk_bf16_f32 v168, v108, v109
	v_cvt_pk_bf16_f32 v169, v110, v111
	v_add_f32_e32 v81, v104, v105
	v_add_f32_e32 v82, v106, v107
	v_add_f32_e32 v83, v108, v109
	v_add_f32_e32 v84, v110, v111
	v_add_f32_e32 v81, v81, v82
	v_add_f32_e32 v83, v83, v84
	v_add_f32_e32 v81, v81, v83
	v_add_f32_e32 v80, v80, v81
	s_waitcnt lgkmcnt(0)
	v_add_u32_e32 v0, s100, v164
	ds_read_b128 v[218:221], v0
	ds_read_b128 v[222:225], v0 offset:8192
	v_mfma_f32_32x32x16_bf16 v[64:79], v[112:115], v[166:169], v[64:79]
	v_mfma_f32_32x32x16_bf16 v[48:63], v[116:119], v[166:169], v[48:63]
	v_mfma_f32_32x32x16_bf16 v[32:47], v[88:91], v[166:169], v[32:47]
	v_mfma_f32_32x32x16_bf16 v[16:31], v[92:95], v[166:169], v[16:31]
	s_mov_b64 s[42:43], 0
	s_mov_b64 s[58:59], -1
	s_and_b64 vcc, exec, s[76:77]
	s_cbranch_vccz .LBB0_833
